# E1-even GEMM epilogue rewritten: rs loads hoisted to unit start (2 rows/lane + bpermute), v_rsq instead of sqrt+div, in-place cvt, MFMA zeroing of accumulators
# speedup vs baseline: 1.0062x; 1.0062x over previous
.LBB0_835:
	s_ashr_i32 s23, s22, 31
	s_lshl_b64 s[8:9], s[22:23], 19
	s_add_u32 s24, s34, s8
	s_addc_u32 s25, s35, s9
	s_and_b64 s[8:9], s[38:39], exec
	s_cselect_b32 s5, s25, s29
	s_cselect_b32 s8, s24, s28
	s_ashr_i32 s21, s20, 31
	s_lshl_b64 s[26:27], s[20:21], 19
	s_add_u32 s26, s36, s26
	s_addc_u32 s27, s37, s27
	s_and_b64 s[30:31], s[38:39], exec
	s_cselect_b32 s9, s27, s7
	s_cselect_b32 s21, s26, s6
	s_add_u32 s23, s6, 0x100
	s_addc_u32 s33, s7, 0
	s_add_u32 s6, s28, 0x40080
	v_mov_b32_e32 v2, 0
	s_addc_u32 s7, s29, 0
	s_mov_b32 s40, -2
	s_cmp_lg_u32 s49, 1
	s_cbranch_scc1 .Lskipz_e1e
	v_mov_b32_e32 v3, v2
	v_mov_b32_e32 v4, v2
	v_mov_b32_e32 v5, v2
	v_mov_b32_e32 v6, v2
	v_mov_b32_e32 v7, v2
	v_mov_b32_e32 v8, v2
	v_mov_b32_e32 v9, v2
	v_mov_b32_e32 v14, v2
	v_mov_b32_e32 v15, v2
	v_mov_b32_e32 v16, v2
	v_mov_b32_e32 v17, v2
	v_mov_b32_e32 v22, v2
	v_mov_b32_e32 v23, v2
	v_mov_b32_e32 v24, v2
	v_mov_b32_e32 v25, v2
	v_mov_b32_e32 v30, v2
	v_mov_b32_e32 v31, v2
	v_mov_b32_e32 v32, v2
	v_mov_b32_e32 v33, v2
	v_mov_b32_e32 v38, v2
	v_mov_b32_e32 v39, v2
	v_mov_b32_e32 v40, v2
	v_mov_b32_e32 v41, v2
	v_mov_b32_e32 v46, v2
	v_mov_b32_e32 v47, v2
	v_mov_b32_e32 v48, v2
	v_mov_b32_e32 v49, v2
	v_mov_b32_e32 v54, v2
	v_mov_b32_e32 v55, v2
	v_mov_b32_e32 v56, v2
	v_mov_b32_e32 v57, v2
	v_mov_b32_e32 v10, v2
	v_mov_b32_e32 v11, v2
	v_mov_b32_e32 v12, v2
	v_mov_b32_e32 v13, v2
	v_mov_b32_e32 v18, v2
	v_mov_b32_e32 v19, v2
	v_mov_b32_e32 v20, v2
	v_mov_b32_e32 v21, v2
	v_mov_b32_e32 v26, v2
	v_mov_b32_e32 v27, v2
	v_mov_b32_e32 v28, v2
	v_mov_b32_e32 v29, v2
	v_mov_b32_e32 v34, v2
	v_mov_b32_e32 v35, v2
	v_mov_b32_e32 v36, v2
	v_mov_b32_e32 v37, v2
	v_mov_b32_e32 v42, v2
	v_mov_b32_e32 v43, v2
	v_mov_b32_e32 v44, v2
	v_mov_b32_e32 v45, v2
	v_mov_b32_e32 v50, v2
	v_mov_b32_e32 v51, v2
	v_mov_b32_e32 v52, v2
	v_mov_b32_e32 v53, v2
	v_mov_b32_e32 v58, v2
	v_mov_b32_e32 v59, v2
	v_mov_b32_e32 v60, v2
	v_mov_b32_e32 v61, v2
	v_mov_b32_e32 v62, v2
	v_mov_b32_e32 v63, v2
	v_mov_b32_e32 v64, v2
	v_mov_b32_e32 v65, v2
	v_mov_b32_e32 v66, v2
	v_mov_b32_e32 v67, v2
	v_mov_b32_e32 v68, v2
	v_mov_b32_e32 v69, v2
	v_mov_b32_e32 v70, v2
	v_mov_b32_e32 v71, v2
	v_mov_b32_e32 v72, v2
	v_mov_b32_e32 v73, v2
	v_mov_b32_e32 v78, v2
	v_mov_b32_e32 v79, v2
	v_mov_b32_e32 v80, v2
	v_mov_b32_e32 v81, v2
	v_mov_b32_e32 v86, v2
	v_mov_b32_e32 v87, v2
	v_mov_b32_e32 v88, v2
	v_mov_b32_e32 v89, v2
	v_mov_b32_e32 v94, v2
	v_mov_b32_e32 v95, v2
	v_mov_b32_e32 v96, v2
	v_mov_b32_e32 v97, v2
	v_mov_b32_e32 v102, v2
	v_mov_b32_e32 v103, v2
	v_mov_b32_e32 v104, v2
	v_mov_b32_e32 v105, v2
	v_mov_b32_e32 v110, v2
	v_mov_b32_e32 v111, v2
	v_mov_b32_e32 v112, v2
	v_mov_b32_e32 v113, v2
	v_mov_b32_e32 v118, v2
	v_mov_b32_e32 v119, v2
	v_mov_b32_e32 v120, v2
	v_mov_b32_e32 v121, v2
	v_mov_b32_e32 v74, v2
	v_mov_b32_e32 v75, v2
	v_mov_b32_e32 v76, v2
	v_mov_b32_e32 v77, v2
	v_mov_b32_e32 v82, v2
	v_mov_b32_e32 v83, v2
	v_mov_b32_e32 v84, v2
	v_mov_b32_e32 v85, v2
	v_mov_b32_e32 v90, v2
	v_mov_b32_e32 v91, v2
	v_mov_b32_e32 v92, v2
	v_mov_b32_e32 v93, v2
	v_mov_b32_e32 v98, v2
	v_mov_b32_e32 v99, v2
	v_mov_b32_e32 v100, v2
	v_mov_b32_e32 v101, v2
	v_mov_b32_e32 v106, v2
	v_mov_b32_e32 v107, v2
	v_mov_b32_e32 v108, v2
	v_mov_b32_e32 v109, v2
	v_mov_b32_e32 v114, v2
	v_mov_b32_e32 v115, v2
	v_mov_b32_e32 v116, v2
	v_mov_b32_e32 v117, v2
	v_mov_b32_e32 v122, v2
	v_mov_b32_e32 v123, v2
	v_mov_b32_e32 v124, v2
	v_mov_b32_e32 v125, v2
	v_mov_b32_e32 v126, v2
	v_mov_b32_e32 v127, v2
	v_mov_b32_e32 v128, v2
	v_mov_b32_e32 v129, v2
.Lskipz_e1e:
	v_and_b32_e32 v130, 8, v187
	v_and_b32_e32 v131, 16, v187
	v_lshlrev_b32_e32 v130, 2, v130
	v_lshl_add_u32 v130, v131, 3, v130
	v_lshl_add_u32 v131, s4, 8, v185
	v_add_u32_e32 v130, v130, v131
	v_mov_b32_e32 v131, 0
	v_lshl_add_u64 v[130:131], v[130:131], 4, s[16:17]
	global_load_dwordx4 v[240:243], v[130:131], off
	global_load_dwordx2 v[244:245], v[130:131], off offset:256
	global_load_dword v184, v[130:131], off offset:264
	global_load_dword v189, v[130:131], off offset:268

.LBB0_839:
	v_mov_b32_e32 v200, 0
	v_mov_b32_e32 v201, 0
	v_mov_b32_e32 v202, 0
	v_mov_b32_e32 v203, 0
	v_lshl_add_u32 v182, s4, 8, v185
	s_lshl_b32 s4, 1, s52
	s_and_b32 s4, s4, 0x18f
	s_cmp_eq_u32 s4, 0
	s_cselect_b64 s[4:5], -1, 0
	v_cndmask_b32_e64 v190, v230, 1.0, s[4:5]
	s_waitcnt vmcnt(8)
	v_add_f32_e32 v240, v240, v241
	v_add_f32_e32 v242, v242, v243
	v_add_f32_e32 v244, v244, v245
	v_add_f32_e32 v184, v184, v189
	v_add_f32_e32 v240, v240, v242
	v_add_f32_e32 v244, v244, v184
	v_fmamk_f32 v240, v240, 0x3a800000, v226
	v_fmamk_f32 v244, v244, 0x3a800000, v226
	v_rsq_f32_e32 v240, v240
	v_rsq_f32_e32 v244, v244
	v_and_b32_e32 v191, 15, v185
	v_lshlrev_b32_e32 v191, 2, v191
	v_add_u32_e32 v192, 64, v191
	v_add_u32_e32 v193, 0x80, v191
	v_add_u32_e32 v194, 0xc0, v191
	v_mul_f32_e32 v240, v240, v190
	v_mul_f32_e32 v244, v244, v190
	ds_bpermute_b32 v144, v191, v240
	ds_bpermute_b32 v146, v191, v244
	ds_bpermute_b32 v148, v192, v240
	ds_bpermute_b32 v150, v192, v244
	ds_bpermute_b32 v152, v193, v240
	ds_bpermute_b32 v154, v193, v244
	ds_bpermute_b32 v156, v194, v240
	ds_bpermute_b32 v168, v194, v244
	s_movk_i32 s6, 0x1a00
	v_lshl_or_b32 v170, s52, 8, v187
	v_lshlrev_b32_e32 v170, 1, v170
	v_mov_b32_e32 v171, 0
	v_mov_b64_e32 v[172:173], s[14:15]
	v_mad_i64_i32 v[172:173], s[4:5], v182, s6, v[172:173]
	v_lshl_add_u64 v[172:173], v[172:173], 0, v[170:171]
	s_waitcnt lgkmcnt(0)
	v_pk_mul_f32 v[126:127], v[126:127], v[144:145] op_sel_hi:[1,0]
	v_pk_mul_f32 v[128:129], v[128:129], v[144:145] op_sel_hi:[1,0]
	v_pk_mul_f32 v[122:123], v[122:123], v[144:145] op_sel_hi:[1,0]
	v_pk_mul_f32 v[124:125], v[124:125], v[144:145] op_sel_hi:[1,0]
	v_cvt_pk_bf16_f32 v126, v126, v127
	v_cvt_pk_bf16_f32 v127, v128, v129
	v_cvt_pk_bf16_f32 v128, v122, v123
	v_cvt_pk_bf16_f32 v129, v124, v125
	global_store_dwordx4 v[172:173], v[126:129], off
	v_pk_mul_f32 v[118:119], v[118:119], v[144:145] op_sel_hi:[1,0]
	v_pk_mul_f32 v[120:121], v[120:121], v[144:145] op_sel_hi:[1,0]
	v_pk_mul_f32 v[110:111], v[110:111], v[144:145] op_sel_hi:[1,0]
	v_pk_mul_f32 v[112:113], v[112:113], v[144:145] op_sel_hi:[1,0]
	v_cvt_pk_bf16_f32 v118, v118, v119
	v_cvt_pk_bf16_f32 v119, v120, v121
	v_cvt_pk_bf16_f32 v120, v110, v111
	v_cvt_pk_bf16_f32 v121, v112, v113
	global_store_dwordx4 v[172:173], v[118:121], off offset:256
	s_mov_b64 s[40:41], 0x1a000
	v_lshl_add_u64 v[176:177], v[172:173], 0, s[40:41]
	v_pk_mul_f32 v[114:115], v[114:115], v[146:147] op_sel_hi:[1,0]
	v_pk_mul_f32 v[116:117], v[116:117], v[146:147] op_sel_hi:[1,0]
	v_pk_mul_f32 v[106:107], v[106:107], v[146:147] op_sel_hi:[1,0]
	v_pk_mul_f32 v[108:109], v[108:109], v[146:147] op_sel_hi:[1,0]
	v_cvt_pk_bf16_f32 v114, v114, v115
	v_cvt_pk_bf16_f32 v115, v116, v117
	v_cvt_pk_bf16_f32 v116, v106, v107
	v_cvt_pk_bf16_f32 v117, v108, v109
	global_store_dwordx4 v[176:177], v[114:117], off
	v_pk_mul_f32 v[102:103], v[102:103], v[146:147] op_sel_hi:[1,0]
	v_pk_mul_f32 v[104:105], v[104:105], v[146:147] op_sel_hi:[1,0]
	v_pk_mul_f32 v[94:95], v[94:95], v[146:147] op_sel_hi:[1,0]
	v_pk_mul_f32 v[96:97], v[96:97], v[146:147] op_sel_hi:[1,0]
	v_cvt_pk_bf16_f32 v102, v102, v103
	v_cvt_pk_bf16_f32 v103, v104, v105
	v_cvt_pk_bf16_f32 v104, v94, v95
	v_cvt_pk_bf16_f32 v105, v96, v97
	global_store_dwordx4 v[176:177], v[102:105], off offset:256
	s_mov_b64 s[40:41], 0x34000
	v_lshl_add_u64 v[174:175], v[172:173], 0, s[40:41]
	v_pk_mul_f32 v[98:99], v[98:99], v[148:149] op_sel_hi:[1,0]
	v_pk_mul_f32 v[100:101], v[100:101], v[148:149] op_sel_hi:[1,0]
	v_pk_mul_f32 v[90:91], v[90:91], v[148:149] op_sel_hi:[1,0]
	v_pk_mul_f32 v[92:93], v[92:93], v[148:149] op_sel_hi:[1,0]
	v_cvt_pk_bf16_f32 v98, v98, v99
	v_cvt_pk_bf16_f32 v99, v100, v101
	v_cvt_pk_bf16_f32 v100, v90, v91
	v_cvt_pk_bf16_f32 v101, v92, v93
	global_store_dwordx4 v[174:175], v[98:101], off
	v_pk_mul_f32 v[86:87], v[86:87], v[148:149] op_sel_hi:[1,0]
	v_pk_mul_f32 v[88:89], v[88:89], v[148:149] op_sel_hi:[1,0]
	v_pk_mul_f32 v[78:79], v[78:79], v[148:149] op_sel_hi:[1,0]
	v_pk_mul_f32 v[80:81], v[80:81], v[148:149] op_sel_hi:[1,0]
	v_cvt_pk_bf16_f32 v86, v86, v87
	v_cvt_pk_bf16_f32 v87, v88, v89
	v_cvt_pk_bf16_f32 v88, v78, v79
	v_cvt_pk_bf16_f32 v89, v80, v81
	global_store_dwordx4 v[174:175], v[86:89], off offset:256
	s_mov_b64 s[40:41], 0x4e000
	v_lshl_add_u64 v[176:177], v[172:173], 0, s[40:41]
	v_pk_mul_f32 v[82:83], v[82:83], v[150:151] op_sel_hi:[1,0]
	v_pk_mul_f32 v[84:85], v[84:85], v[150:151] op_sel_hi:[1,0]
	v_pk_mul_f32 v[74:75], v[74:75], v[150:151] op_sel_hi:[1,0]
	v_pk_mul_f32 v[76:77], v[76:77], v[150:151] op_sel_hi:[1,0]
	v_cvt_pk_bf16_f32 v82, v82, v83
	v_cvt_pk_bf16_f32 v83, v84, v85
	v_cvt_pk_bf16_f32 v84, v74, v75
	v_cvt_pk_bf16_f32 v85, v76, v77
	global_store_dwordx4 v[176:177], v[82:85], off
	v_pk_mul_f32 v[70:71], v[70:71], v[150:151] op_sel_hi:[1,0]
	v_pk_mul_f32 v[72:73], v[72:73], v[150:151] op_sel_hi:[1,0]
	v_pk_mul_f32 v[66:67], v[66:67], v[150:151] op_sel_hi:[1,0]
	v_pk_mul_f32 v[68:69], v[68:69], v[150:151] op_sel_hi:[1,0]
	v_cvt_pk_bf16_f32 v70, v70, v71
	v_cvt_pk_bf16_f32 v71, v72, v73
	v_cvt_pk_bf16_f32 v72, v66, v67
	v_cvt_pk_bf16_f32 v73, v68, v69
	global_store_dwordx4 v[176:177], v[70:73], off offset:256
	s_mov_b64 s[40:41], 0xd0000
	v_lshl_add_u64 v[174:175], v[172:173], 0, s[40:41]
	v_pk_mul_f32 v[62:63], v[62:63], v[152:153] op_sel_hi:[1,0]
	v_pk_mul_f32 v[64:65], v[64:65], v[152:153] op_sel_hi:[1,0]
	v_pk_mul_f32 v[58:59], v[58:59], v[152:153] op_sel_hi:[1,0]
	v_pk_mul_f32 v[60:61], v[60:61], v[152:153] op_sel_hi:[1,0]
	v_cvt_pk_bf16_f32 v62, v62, v63
	v_cvt_pk_bf16_f32 v63, v64, v65
	v_cvt_pk_bf16_f32 v64, v58, v59
	v_cvt_pk_bf16_f32 v65, v60, v61
	global_store_dwordx4 v[174:175], v[62:65], off
	v_pk_mul_f32 v[54:55], v[54:55], v[152:153] op_sel_hi:[1,0]
	v_pk_mul_f32 v[56:57], v[56:57], v[152:153] op_sel_hi:[1,0]
	v_pk_mul_f32 v[46:47], v[46:47], v[152:153] op_sel_hi:[1,0]
	v_pk_mul_f32 v[48:49], v[48:49], v[152:153] op_sel_hi:[1,0]
	v_cvt_pk_bf16_f32 v54, v54, v55
	v_cvt_pk_bf16_f32 v55, v56, v57
	v_cvt_pk_bf16_f32 v56, v46, v47
	v_cvt_pk_bf16_f32 v57, v48, v49
	global_store_dwordx4 v[174:175], v[54:57], off offset:256
	s_mov_b64 s[40:41], 0xea000
	v_lshl_add_u64 v[176:177], v[172:173], 0, s[40:41]
	v_pk_mul_f32 v[50:51], v[50:51], v[154:155] op_sel_hi:[1,0]
	v_pk_mul_f32 v[52:53], v[52:53], v[154:155] op_sel_hi:[1,0]
	v_pk_mul_f32 v[42:43], v[42:43], v[154:155] op_sel_hi:[1,0]
	v_pk_mul_f32 v[44:45], v[44:45], v[154:155] op_sel_hi:[1,0]
	v_cvt_pk_bf16_f32 v50, v50, v51
	v_cvt_pk_bf16_f32 v51, v52, v53
	v_cvt_pk_bf16_f32 v52, v42, v43
	v_cvt_pk_bf16_f32 v53, v44, v45
	global_store_dwordx4 v[176:177], v[50:53], off
	v_pk_mul_f32 v[38:39], v[38:39], v[154:155] op_sel_hi:[1,0]
	v_pk_mul_f32 v[40:41], v[40:41], v[154:155] op_sel_hi:[1,0]
	v_pk_mul_f32 v[30:31], v[30:31], v[154:155] op_sel_hi:[1,0]
	v_pk_mul_f32 v[32:33], v[32:33], v[154:155] op_sel_hi:[1,0]
	v_cvt_pk_bf16_f32 v38, v38, v39
	v_cvt_pk_bf16_f32 v39, v40, v41
	v_cvt_pk_bf16_f32 v40, v30, v31
	v_cvt_pk_bf16_f32 v41, v32, v33
	global_store_dwordx4 v[176:177], v[38:41], off offset:256
	s_mov_b64 s[40:41], 0x104000
	v_lshl_add_u64 v[174:175], v[172:173], 0, s[40:41]
	v_pk_mul_f32 v[34:35], v[34:35], v[156:157] op_sel_hi:[1,0]
	v_pk_mul_f32 v[36:37], v[36:37], v[156:157] op_sel_hi:[1,0]
	v_pk_mul_f32 v[26:27], v[26:27], v[156:157] op_sel_hi:[1,0]
	v_pk_mul_f32 v[28:29], v[28:29], v[156:157] op_sel_hi:[1,0]
	v_cvt_pk_bf16_f32 v34, v34, v35
	v_cvt_pk_bf16_f32 v35, v36, v37
	v_cvt_pk_bf16_f32 v36, v26, v27
	v_cvt_pk_bf16_f32 v37, v28, v29
	global_store_dwordx4 v[174:175], v[34:37], off
	v_pk_mul_f32 v[22:23], v[22:23], v[156:157] op_sel_hi:[1,0]
	v_pk_mul_f32 v[24:25], v[24:25], v[156:157] op_sel_hi:[1,0]
	v_pk_mul_f32 v[14:15], v[14:15], v[156:157] op_sel_hi:[1,0]
	v_pk_mul_f32 v[16:17], v[16:17], v[156:157] op_sel_hi:[1,0]
	v_cvt_pk_bf16_f32 v22, v22, v23
	v_cvt_pk_bf16_f32 v23, v24, v25
	v_cvt_pk_bf16_f32 v24, v14, v15
	v_cvt_pk_bf16_f32 v25, v16, v17
	global_store_dwordx4 v[174:175], v[22:25], off offset:256
	s_mov_b64 s[40:41], 0x11e000
	v_lshl_add_u64 v[176:177], v[172:173], 0, s[40:41]
	v_pk_mul_f32 v[18:19], v[18:19], v[168:169] op_sel_hi:[1,0]
	v_pk_mul_f32 v[20:21], v[20:21], v[168:169] op_sel_hi:[1,0]
	v_pk_mul_f32 v[10:11], v[10:11], v[168:169] op_sel_hi:[1,0]
	v_pk_mul_f32 v[12:13], v[12:13], v[168:169] op_sel_hi:[1,0]
	v_cvt_pk_bf16_f32 v18, v18, v19
	v_cvt_pk_bf16_f32 v19, v20, v21
	v_cvt_pk_bf16_f32 v20, v10, v11
	v_cvt_pk_bf16_f32 v21, v12, v13
	global_store_dwordx4 v[176:177], v[18:21], off
	v_pk_mul_f32 v[6:7], v[6:7], v[168:169] op_sel_hi:[1,0]
	v_pk_mul_f32 v[8:9], v[8:9], v[168:169] op_sel_hi:[1,0]
	v_pk_mul_f32 v[2:3], v[2:3], v[168:169] op_sel_hi:[1,0]
	v_pk_mul_f32 v[4:5], v[4:5], v[168:169] op_sel_hi:[1,0]
	v_cvt_pk_bf16_f32 v6, v6, v7
	v_cvt_pk_bf16_f32 v7, v8, v9
	v_cvt_pk_bf16_f32 v8, v2, v3
	v_cvt_pk_bf16_f32 v9, v4, v5
	global_store_dwordx4 v[176:177], v[6:9], off offset:256
	s_nop 3
	v_mfma_f32_32x32x16_bf16 v[2:17], v[200:203], v[200:203], 0
	v_mfma_f32_32x32x16_bf16 v[18:33], v[200:203], v[200:203], 0
	v_mfma_f32_32x32x16_bf16 v[34:49], v[200:203], v[200:203], 0
	v_mfma_f32_32x32x16_bf16 v[50:65], v[200:203], v[200:203], 0
	v_mfma_f32_32x32x16_bf16 v[66:81], v[200:203], v[200:203], 0
	v_mfma_f32_32x32x16_bf16 v[82:97], v[200:203], v[200:203], 0
	v_mfma_f32_32x32x16_bf16 v[98:113], v[200:203], v[200:203], 0
	v_mfma_f32_32x32x16_bf16 v[114:129], v[200:203], v[200:203], 0
	s_andn2_b64 vcc, exec, s[38:39]
	s_mov_b64 s[6:7], -1
	s_cbranch_vccnz .LBB0_832
	s_andn2_b64 vcc, exec, s[12:13]
	s_cbranch_vccnz .LBB0_831
	s_barrier
	s_branch .LBB0_831
